# baseline (speedup 1.0000x reference)
_Z11attn_kernelPKDF16_S0_S0_PDF16_P15HIP_vector_typeIfLj2EE:
	s_mov_b32 s28, s2
	s_load_dwordx4 s[32:35], s[0:1], 0x8
	v_readfirstlane_b32 s3, v0
	s_ashr_i32 s12, s2, 5
	s_lshr_b32 s21, s3, 6
	s_and_b32 s3, s2, 7
	s_and_b32 s12, s12, -8
	s_load_dwordx8 s[4:11], s[0:1], 0x0
	s_or_b32 s12, s12, s3
	s_bfe_u32 s20, s2, 0x10003
	s_lshl_b32 s2, s2, 3
	s_and_b32 s2, s2, 0x780
	s_lshl_b32 s3, s21, 5
	s_ashr_i32 s13, s12, 31
	s_add_i32 s2, s3, s2
	s_lshl_b64 s[16:17], s[12:13], 11
	s_lshl_b32 s3, s20, 10
	s_or_b32 s14, s16, s3
	s_mov_b32 s15, s17
	s_lshl_b64 s[18:19], s[14:15], 7
	s_lshl_b64 s[14:15], s[12:13], 18
	s_waitcnt lgkmcnt(0)
	s_add_u32 s3, s8, s14
	s_addc_u32 s22, s9, s15
	s_add_u32 s16, s16, s2
	v_and_b32_e32 v98, 31, v0
	s_addc_u32 s17, s17, 0
	v_or_b32_e32 v2, s16, v98
	v_mov_b32_e32 v3, s17
	v_bfe_u32 v54, v0, 5, 1
	v_lshlrev_b64 v[2:3], 7, v[2:3]
	v_mov_b32_e32 v51, 0
	v_lshl_add_u64 v[2:3], s[4:5], 0, v[2:3]
	v_lshlrev_b32_e32 v50, 4, v54
	v_lshl_add_u64 v[2:3], v[2:3], 0, v[50:51]
	s_add_u32 s18, s6, s18
	v_bfe_u32 v1, v0, 3, 3
	global_load_dwordx4 v[94:97], v[2:3], off nt
	global_load_dwordx4 v[90:93], v[2:3], off offset:32 nt
	global_load_dwordx4 v[86:89], v[2:3], off offset:64 nt
	global_load_dwordx4 v[82:85], v[2:3], off offset:96 nt
	s_addc_u32 s19, s7, s19
	s_lshl_b32 s24, s20, 11
	v_lshl_or_b32 v2, s21, 4, v1
	v_and_b32_e32 v99, 63, v0
	s_add_u32 s4, s3, s24
	v_or_b32_e32 v3, 8, v2
	v_lshlrev_b32_e32 v4, 4, v0
	s_movk_i32 s3, 0x70
	v_bitop3_b32 v53, v99, s3, v4 bitop3:0x48
	v_lshrrev_b32_e32 v4, 1, v3
	v_xor_b32_e32 v4, v4, v0
	s_addc_u32 s5, s22, 0
	v_lshlrev_b32_e32 v4, 4, v4
	s_lshl_b32 s22, s21, 11
	v_and_b32_e32 v52, 0x70, v4
	v_lshl_or_b32 v55, v2, 7, v53
	s_mov_b32 m0, s22
	v_lshl_or_b32 v64, v3, 7, v52
	global_load_lds_dwordx4 v55, s[18:19]
	s_or_b32 m0, s22, 0x400
	v_lshl_or_b32 v50, v2, 12, v53
	global_load_lds_dwordx4 v64, s[18:19]
	s_add_i32 m0, s22, 0x2000
	v_lshl_or_b32 v2, v3, 12, v52
	global_load_lds_dwordx4 v50, s[4:5]
	s_add_i32 m0, s22, 0x2400
	v_mov_b32_e32 v3, v51
	global_load_lds_dwordx4 v2, s[4:5]
	s_add_i32 m0, s22, 0x4000
	v_lshl_add_u64 v[60:61], s[4:5], 0, v[50:51]
	v_lshl_add_u64 v[62:63], s[4:5], 0, v[2:3]
	s_add_u32 s4, s18, 0x2000
	s_addc_u32 s5, s19, 0
	s_add_i32 m0, s22, 0x4400
	s_load_dwordx2 s[0:1], s[0:1], 0x20
	s_mov_b64 s[4:5], 0x80
	v_lshl_add_u64 v[2:3], v[60:61], 0, s[4:5]
	s_add_i32 m0, s22, 0x6000
	v_lshrrev_b32_e32 v4, 1, v0
	v_lshl_add_u64 v[2:3], v[62:63], 0, s[4:5]
	s_add_i32 m0, s22, 0x6400
	v_and_b32_e32 v5, 4, v4
	v_lshlrev_b32_e32 v3, 1, v0
	v_and_b32_e32 v2, 19, v0
	v_and_b32_e32 v3, 8, v3
	v_or3_b32 v2, v3, v2, v5
	s_waitcnt vmcnt(0)
	v_lshlrev_b32_e32 v115, 7, v2
	v_lshrrev_b32_e32 v3, 1, v2
	v_bfe_u32 v46, v2, 1, 3
	v_bitop3_b32 v2, v54, v4, 7 bitop3:0x78
	s_mov_b32 s3, 0
	v_lshlrev_b32_e32 v108, 3, v54
	s_mov_b32 s23, 1
	s_mov_b64 s[16:17], 0x2000
	v_lshlrev_b32_e32 v109, 7, v98
	v_lshlrev_b32_e32 v110, 4, v2
	s_movk_i32 s25, 0x400
	v_bfe_u32 v50, v0, 1, 3
	s_barrier
	s_and_b32 s29, s28, 7
	s_lshr_b32 s40, s28, 3
	s_lshr_b32 s41, s40, 5
	s_lshl_b32 s41, s41, 3
	s_or_b32 s29, s41, s29
	s_and_b32 s40, s40, 1
	s_lshl_b32 s29, s29, 18
	s_lshl_b32 s41, s40, 17
	s_lshl_b32 s42, s40, 11
	s_add_i32 s41, s41, s29
	s_add_i32 s41, s41, 0x6000
	s_add_i32 s42, s42, s29
	s_add_i32 s42, s42, 0x180
	v_and_b32_e32 v145, 63, v0
	v_lshrrev_b32_e32 v146, 3, v145
	v_lshl_add_u32 v146, s21, 4, v146
	v_and_b32_e32 v145, 7, v145
	v_bfe_u32 v147, v146, 1, 3
	v_xor_b32_e32 v148, v145, v147
	v_xor_b32_e32 v147, 4, v148
	v_lshlrev_b32_e32 v148, 4, v148
	v_lshlrev_b32_e32 v147, 4, v147
	v_lshl_add_u32 v145, v146, 7, v148
	v_lshl_add_u32 v149, v146, 7, v147
	v_add_u32_e32 v149, 0x400, v149
	v_lshl_add_u32 v148, v146, 12, v148
	v_lshl_add_u32 v147, v146, 12, v147
	v_add_u32_e32 v147, 0x8000, v147
	s_waitcnt lgkmcnt(0)
	s_add_u32 s36, s32, s41
	s_addc_u32 s37, s33, 0
	s_add_u32 s38, s34, s42
	s_addc_u32 s39, s35, 0
	s_sub_u32 s40, s36, 0x4000
	s_subb_u32 s41, s37, 0
	s_sub_u32 s42, s38, 0x100
	s_subb_u32 s43, s39, 0
	s_add_i32 m0, s22, 0x4000
	s_nop 0
	global_load_lds_dwordx4 v145, s[40:41]
	s_add_i32 m0, s22, 0x4400
	s_nop 0
	global_load_lds_dwordx4 v149, s[40:41]
	s_add_i32 m0, s22, 0x6000
	s_nop 0
	global_load_lds_dwordx4 v148, s[42:43]
	s_add_i32 m0, s22, 0x6400
	s_nop 0
	global_load_lds_dwordx4 v147, s[42:43]
	v_bitop3_b32 v2, v54, v3, 7 bitop3:0x78
	v_lshlrev_b32_e32 v116, 4, v2
	v_bitop3_b32 v6, v54, v46, 2 bitop3:0x36
	v_lshlrev_b32_e32 v117, 4, v6
	v_bitop3_b32 v42, v54, v46, 4 bitop3:0x36
	v_bitop3_b32 v46, v54, v46, 6 bitop3:0x36
	v_lshlrev_b32_e32 v118, 4, v42
	v_lshlrev_b32_e32 v119, 4, v46
	v_bitop3_b32 v10, v54, v50, 2 bitop3:0x36
	v_lshlrev_b32_e32 v112, 4, v10
	v_bitop3_b32 v55, v54, v50, 4 bitop3:0x36
	v_bitop3_b32 v50, v54, v50, 6 bitop3:0x36
	v_lshlrev_b32_e32 v111, 4, v55
	v_lshlrev_b32_e32 v113, 4, v50
	v_mov_b32_e32 v2, 0
	v_mov_b32_e32 v3, 0
	v_mov_b32_e32 v4, 0
	v_mov_b32_e32 v5, 0
	v_mov_b32_e32 v6, 0
	v_mov_b32_e32 v7, 0
	v_mov_b32_e32 v8, 0
	v_mov_b32_e32 v9, 0
	v_mov_b32_e32 v10, 0
	v_mov_b32_e32 v11, 0
	v_mov_b32_e32 v12, 0
	v_mov_b32_e32 v13, 0
	v_mov_b32_e32 v14, 0
	v_mov_b32_e32 v15, 0
	v_mov_b32_e32 v16, 0
	v_mov_b32_e32 v17, 0
	v_mov_b32_e32 v18, 0
	v_mov_b32_e32 v19, 0
	v_mov_b32_e32 v20, 0
	v_mov_b32_e32 v21, 0
	v_mov_b32_e32 v22, 0
	v_mov_b32_e32 v23, 0
	v_mov_b32_e32 v24, 0
	v_mov_b32_e32 v25, 0
	v_mov_b32_e32 v26, 0
	v_mov_b32_e32 v27, 0
	v_mov_b32_e32 v28, 0
	v_mov_b32_e32 v29, 0
	v_mov_b32_e32 v30, 0
	v_mov_b32_e32 v31, 0
	v_mov_b32_e32 v32, 0
	v_mov_b32_e32 v33, 0
	v_mov_b32_e32 v34, 0
	v_mov_b32_e32 v35, 0
	v_mov_b32_e32 v36, 0
	v_mov_b32_e32 v37, 0
	v_mov_b32_e32 v38, 0
	v_mov_b32_e32 v39, 0
	v_mov_b32_e32 v40, 0
	v_mov_b32_e32 v41, 0
	v_mov_b32_e32 v42, 0
	v_mov_b32_e32 v43, 0
	v_mov_b32_e32 v44, 0
	v_mov_b32_e32 v45, 0
	v_mov_b32_e32 v46, 0
	v_mov_b32_e32 v47, 0
	v_mov_b32_e32 v48, 0
	v_mov_b32_e32 v49, 0
	v_mov_b32_e32 v114, 0
	s_mov_b32 s23, 0
	s_mov_b32 s9, 0
	s_mov_b32 s8, 0x46000000
	s_sub_u32 s36, s36, 0x2000
	s_subb_u32 s37, s37, 0
	s_sub_u32 s38, s38, 0x80
	s_subb_u32 s39, s39, 0
	s_mov_b32 s44, 0xff800000
	s_mov_b32 s45, 0x3c800000

.LBB3_5:
.LBB3_6:
	v_add_u32_e32 v167, s18, v109
	v_add_u32_e32 v166, v167, v110
	ds_read_b128 v[158:161], v166 offset:8192
	ds_read_b128 v[162:165], v166 offset:12288
	s_nop 0
	v_exp_f32_e32 v120, v66
	v_exp_f32_e32 v121, v67
	v_exp_f32_e32 v122, v68
	v_exp_f32_e32 v123, v69
	v_exp_f32_e32 v124, v70
	v_exp_f32_e32 v125, v71
	v_exp_f32_e32 v126, v72
	v_exp_f32_e32 v127, v73
	v_exp_f32_e32 v128, v74
	v_exp_f32_e32 v129, v75
	v_exp_f32_e32 v130, v76
	v_exp_f32_e32 v131, v77
	v_exp_f32_e32 v132, v78
	v_exp_f32_e32 v133, v79
	v_exp_f32_e32 v134, v80
	v_exp_f32_e32 v135, v81
	v_exp_f32_e32 v136, v50
	v_exp_f32_e32 v137, v51
	v_exp_f32_e32 v138, v52
	v_exp_f32_e32 v139, v53
	v_exp_f32_e32 v140, v54
	v_exp_f32_e32 v141, v55
	v_exp_f32_e32 v142, v56
	v_exp_f32_e32 v143, v57
	v_exp_f32_e32 v150, v58
	v_exp_f32_e32 v151, v59
	v_exp_f32_e32 v152, v60
	v_exp_f32_e32 v153, v61
	v_exp_f32_e32 v154, v62
	v_exp_f32_e32 v155, v63
	v_exp_f32_e32 v156, v64
	v_exp_f32_e32 v157, v65
	v_add_f32_e32 v144, v120, v121
	v_add_f32_e32 v166, v122, v123
	v_add_f32_e32 v144, v144, v124
	v_add_f32_e32 v166, v166, v125
	v_add_f32_e32 v144, v144, v126
	v_add_f32_e32 v166, v166, v127
	v_add_f32_e32 v144, v144, v128
	v_add_f32_e32 v166, v166, v129
	v_add_f32_e32 v144, v144, v130
	v_add_f32_e32 v166, v166, v131
	v_add_f32_e32 v144, v144, v132
	v_add_f32_e32 v166, v166, v133
	v_add_f32_e32 v144, v144, v134
	v_add_f32_e32 v166, v166, v135
	v_add_f32_e32 v144, v144, v136
	v_add_f32_e32 v166, v166, v137
	v_add_f32_e32 v144, v144, v138
	v_add_f32_e32 v166, v166, v139
	v_add_f32_e32 v144, v144, v140
	v_add_f32_e32 v166, v166, v141
	v_add_f32_e32 v144, v144, v142
	v_add_f32_e32 v166, v166, v143
	v_add_f32_e32 v144, v144, v150
	v_add_f32_e32 v166, v166, v151
	v_add_f32_e32 v144, v144, v152
	v_add_f32_e32 v166, v166, v153
	v_add_f32_e32 v144, v144, v154
	v_add_f32_e32 v166, v166, v155
	v_add_f32_e32 v144, v144, v156
	v_add_f32_e32 v166, v166, v157
	v_add_f32_e32 v144, v144, v166
	s_nop 0
	v_cmp_lt_f32_e32 vcc, s8, v144
	v_cmp_gt_f32_e64 s[46:47], s45, v144
	s_or_b64 vcc, vcc, s[46:47]
	s_cbranch_vccnz .Lattn_slow
	s_mov_b32 s44, 0
	s_mov_b32 s45, 0xbf800000
	v_add_u32_e32 v166, v167, v112
	ds_read_b128 v[50:53], v166 offset:8192
	ds_read_b128 v[54:57], v166 offset:12288
	s_add_i32 s9, s9, 1
	s_add_i32 s6, s23, 1
	s_cmp_lg_u32 s23, 2
	s_cselect_b32 s23, s6, 0
	v_cvt_pk_f16_f32 v66, v120, v121
	v_cvt_pk_f16_f32 v67, v122, v123
	v_cvt_pk_f16_f32 v68, v124, v125
	v_cvt_pk_f16_f32 v69, v126, v127
	v_cvt_pk_f16_f32 v70, v128, v129
	v_cvt_pk_f16_f32 v71, v130, v131
	v_cvt_pk_f16_f32 v72, v132, v133
	v_cvt_pk_f16_f32 v73, v134, v135
	v_add_u32_e32 v166, v167, v111
	v_add_u32_e32 v167, v167, v113
	s_waitcnt lgkmcnt(2)
	s_setprio 1
	v_mfma_f32_32x32x16_f16 v[18:33], v[158:161], v[66:69], v[18:33]
	v_mfma_f32_32x32x16_f16 v[2:17], v[162:165], v[66:69], v[2:17]
	ds_read_b128 v[58:61], v166 offset:8192
	ds_read_b128 v[62:65], v166 offset:12288
	v_cvt_pk_f16_f32 v74, v136, v137
	v_cvt_pk_f16_f32 v75, v138, v139
	v_cvt_pk_f16_f32 v76, v140, v141
	v_cvt_pk_f16_f32 v77, v142, v143
	s_waitcnt lgkmcnt(2)
	v_mfma_f32_32x32x16_f16 v[18:33], v[50:53], v[70:73], v[18:33]
	v_mfma_f32_32x32x16_f16 v[2:17], v[54:57], v[70:73], v[2:17]
	ds_read_b128 v[120:123], v167 offset:8192
	ds_read_b128 v[124:127], v167 offset:12288
	v_cvt_pk_f16_f32 v78, v150, v151
	v_cvt_pk_f16_f32 v79, v152, v153
	v_cvt_pk_f16_f32 v80, v154, v155
	v_cvt_pk_f16_f32 v81, v156, v157
	v_add_f32_e32 v114, v114, v144
	s_waitcnt lgkmcnt(2)
	v_mfma_f32_32x32x16_f16 v[18:33], v[58:61], v[74:77], v[18:33]
	v_mfma_f32_32x32x16_f16 v[2:17], v[62:65], v[74:77], v[2:17]
	s_waitcnt lgkmcnt(0)
	v_mfma_f32_32x32x16_f16 v[18:33], v[120:123], v[78:81], v[18:33]
	v_mfma_f32_32x32x16_f16 v[2:17], v[124:127], v[78:81], v[2:17]
	s_setprio 0
	s_cmp_eq_u32 s9, 15
	s_cbranch_scc0 .LBB3_1
	s_branch .LBB3_8
.Lattn_slow:
	s_mov_b32 s45, 0xbf800000
	v_max3_f32 v120, v66, v67, v68
	v_max3_f32 v120, v120, v69, v70
	v_max3_f32 v120, v120, v71, v72
	v_max3_f32 v120, v120, v73, v74
	v_max3_f32 v120, v120, v75, v76
	v_max3_f32 v120, v120, v77, v78
	v_max3_f32 v120, v120, v79, v80
	v_max_f32 v120, v120, v81
	v_max3_f32 v121, v50, v51, v52
	v_max3_f32 v121, v121, v53, v54
	v_max3_f32 v121, v121, v55, v56
	v_max3_f32 v121, v121, v57, v58
	v_max3_f32 v121, v121, v59, v60
	v_max3_f32 v121, v121, v61, v62
	v_max3_f32 v121, v121, v63, v64
	v_max_f32 v121, v121, v65
	s_nop 0
	v_max3_f32 v120, v120, v121, v121
	s_nop 0
	v_mov_b32_e32 v121, v120
	s_nop 1
	v_permlane32_swap_b32_e32 v120, v121
	v_max3_f32 v120, v120, v121, v121
	s_nop 0
.LBB3_7:
	v_max_f32_e32 v120, v120, v120
	v_max_f32_e32 v121, s44, v120
	v_exp_f32_e64 v120, -v121
	v_sub_f32_e32 v66, v66, v121
	v_sub_f32_e32 v67, v67, v121
	v_sub_f32_e32 v68, v68, v121
	v_pk_mul_f32 v[32:33], v[120:121], v[32:33] op_sel_hi:[0,1]
	v_pk_mul_f32 v[30:31], v[120:121], v[30:31] op_sel_hi:[0,1]
	v_pk_mul_f32 v[28:29], v[120:121], v[28:29] op_sel_hi:[0,1]
	v_pk_mul_f32 v[26:27], v[120:121], v[26:27] op_sel_hi:[0,1]
	v_pk_mul_f32 v[24:25], v[120:121], v[24:25] op_sel_hi:[0,1]
	v_pk_mul_f32 v[22:23], v[120:121], v[22:23] op_sel_hi:[0,1]
	v_pk_mul_f32 v[20:21], v[120:121], v[20:21] op_sel_hi:[0,1]
	v_pk_mul_f32 v[18:19], v[120:121], v[18:19] op_sel_hi:[0,1]
	v_pk_mul_f32 v[16:17], v[120:121], v[16:17] op_sel_hi:[0,1]
	v_pk_mul_f32 v[14:15], v[120:121], v[14:15] op_sel_hi:[0,1]
	v_pk_mul_f32 v[12:13], v[120:121], v[12:13] op_sel_hi:[0,1]
	v_pk_mul_f32 v[10:11], v[120:121], v[10:11] op_sel_hi:[0,1]
	v_pk_mul_f32 v[8:9], v[120:121], v[8:9] op_sel_hi:[0,1]
	v_pk_mul_f32 v[6:7], v[120:121], v[6:7] op_sel_hi:[0,1]
	v_pk_mul_f32 v[4:5], v[120:121], v[4:5] op_sel_hi:[0,1]
	v_pk_mul_f32 v[2:3], v[120:121], v[2:3] op_sel_hi:[0,1]
	v_sub_f32_e32 v69, v69, v121
	v_sub_f32_e32 v70, v70, v121
	v_sub_f32_e32 v71, v71, v121
	v_sub_f32_e32 v72, v72, v121
	v_sub_f32_e32 v73, v73, v121
	v_sub_f32_e32 v74, v74, v121
	v_sub_f32_e32 v75, v75, v121
	v_sub_f32_e32 v76, v76, v121
	v_sub_f32_e32 v77, v77, v121
	v_sub_f32_e32 v78, v78, v121
	v_sub_f32_e32 v79, v79, v121
	v_sub_f32_e32 v80, v80, v121
	v_sub_f32_e32 v81, v81, v121
	v_sub_f32_e32 v50, v50, v121
	v_sub_f32_e32 v51, v51, v121
	v_sub_f32_e32 v52, v52, v121
	v_sub_f32_e32 v53, v53, v121
	v_sub_f32_e32 v54, v54, v121
	v_sub_f32_e32 v55, v55, v121
	v_sub_f32_e32 v56, v56, v121
	v_sub_f32_e32 v57, v57, v121
	v_sub_f32_e32 v58, v58, v121
	v_sub_f32_e32 v59, v59, v121
	v_sub_f32_e32 v60, v60, v121
	v_sub_f32_e32 v61, v61, v121
	v_sub_f32_e32 v62, v62, v121
	v_sub_f32_e32 v63, v63, v121
	v_sub_f32_e32 v64, v64, v121
	v_sub_f32_e32 v65, v65, v121
	v_sub_f32_e32 v49, v49, v121
	v_sub_f32_e32 v48, v48, v121
	v_sub_f32_e32 v47, v47, v121
	v_sub_f32_e32 v46, v46, v121
	v_sub_f32_e32 v45, v45, v121
	v_sub_f32_e32 v44, v44, v121
	v_sub_f32_e32 v43, v43, v121
	v_sub_f32_e32 v42, v42, v121
	v_sub_f32_e32 v41, v41, v121
	v_sub_f32_e32 v40, v40, v121
	v_sub_f32_e32 v39, v39, v121
	v_sub_f32_e32 v38, v38, v121
	v_sub_f32_e32 v37, v37, v121
	v_sub_f32_e32 v36, v36, v121
	v_sub_f32_e32 v35, v35, v121
	v_sub_f32_e32 v34, v34, v121
	v_mul_f32_e32 v114, v114, v120
	s_mov_b32 s44, 0
	s_branch .LBB3_6
